# conv+SiLU phase: bf16 pair packing by v_cvt_pk_bf16_f32 instead of the 6-instruction integer RNE sequence (320 VALU fewer per item)
# speedup vs baseline: 1.0150x; 1.0049x over previous
; __device__ __forceinline__ unsigned pk2(float lo, float hi) { return f2bf(lo) | (f2bf(hi) << 16); }
; __device__ __forceinline__ float bflo(unsigned w) { return __uint_as_float(w << 16); }
; __device__ __forceinline__ float bfhi(unsigned w) { return __uint_as_float(w & 0xffff0000u); }
; __device__ __forceinline__ float sigmoidf_(float x) { return frcp_(1.0f + fexp_(-x)); }
; __device__ __forceinline__ void p3_conv(const Args& a, const Frame& F) {
;     ...
;         for (int i = 0; i < 16; ++i) {
;             const unsigned wm[4] = {rw[i].x, rw[i].y, rw[i].z, rw[i].w}, wc_[4] = {rw[i + 1].x, rw[i + 1].y, rw[i + 1].z, rw[i + 1].w}, wp[4] = {rw[i + 2].x, rw[i + 2].y, rw[i + 2].z, rw[i + 2].w};
;             float o[8];
; #pragma unroll
;             for (int j = 0; j < 4; ++j) {
;                 const float a0 = bb[2 * j] + bflo(wm[j]) * w0[2 * j] + bflo(wc_[j]) * w1[2 * j] + bflo(wp[j]) * w2[2 * j];
;                 const float a1 = bb[2 * j + 1] + bfhi(wm[j]) * w0[2 * j + 1] + bfhi(wc_[j]) * w1[2 * j + 1] + bfhi(wp[j]) * w2[2 * j + 1];
;                 o[2 * j] = a0 * sigmoidf_(a0) * scl; o[2 * j + 1] = a1 * sigmoidf_(a1) * scl; }
;             u32x4 w; w.x = pk2(o[0], o[1]); w.y = pk2(o[2], o[3]); w.z = pk2(o[4], o[5]); w.w = pk2(o[6], o[7]);
;             *(u32x4*)(QKC + (size_t)(r0 + i) * 1024 + c0) = w;
.LBB0_343:
	s_or_b64 exec, exec, s[8:9]
	s_waitcnt vmcnt(0)
	v_lshlrev_b32_e32 v153, 16, v97
	v_lshlrev_b32_e32 v152, 16, v96
	v_and_b32_e32 v97, 0xffff0000, v97
	v_and_b32_e32 v96, 0xffff0000, v96
	v_lshlrev_b32_e32 v150, 16, v100
	v_and_b32_e32 v100, 0xffff0000, v100
	v_lshlrev_b32_e32 v151, 16, v101
	v_and_b32_e32 v101, 0xffff0000, v101
	v_pk_fma_f32 v[96:97], v[114:115], v[96:97], v[112:113]
	v_pk_fma_f32 v[152:153], v[10:11], v[152:153], v[6:7]
	v_pk_fma_f32 v[96:97], v[4:5], v[100:101], v[96:97]
	v_and_b32_e32 v161, 0xffff0000, v93
	v_and_b32_e32 v160, 0xffff0000, v92
	v_pk_fma_f32 v[152:153], v[18:19], v[150:151], v[152:153]
	v_lshlrev_b32_e32 v159, 16, v93
	v_lshlrev_b32_e32 v158, 16, v92
	v_pk_fma_f32 v[92:93], v[16:17], v[160:161], v[96:97]
	v_pk_fma_f32 v[152:153], v[22:23], v[158:159], v[152:153]
	v_mul_f32_e32 v96, 0xbfb8aa3b, v92
	v_mul_f32_e32 v107, 0xbfb8aa3b, v152
	v_exp_f32_e32 v97, v96
	v_mul_f32_e32 v96, 0xbfb8aa3b, v153
	v_exp_f32_e32 v107, v107
	v_exp_f32_e32 v162, v96
	v_lshlrev_b32_e32 v157, 16, v99
	v_lshlrev_b32_e32 v156, 16, v98
	v_add_f32_e32 v96, 1.0, v107
	v_add_f32_e32 v107, 1.0, v97
	v_add_f32_e32 v97, 1.0, v162
	v_rcp_f32_e32 v96, v96
	v_rcp_f32_e32 v97, v97
	v_mul_f32_e32 v162, 0xbfb8aa3b, v93
	v_exp_f32_e32 v163, v162
	v_lshlrev_b32_e32 v154, 16, v102
	v_lshlrev_b32_e32 v155, 16, v103
	v_pk_mul_f32 v[96:97], v[152:153], v[96:97]
	v_pk_fma_f32 v[152:153], v[14:15], v[156:157], v[2:3]
	v_lshlrev_b32_e32 v157, 16, v95
	v_pk_fma_f32 v[152:153], v[26:27], v[154:155], v[152:153]
	v_lshlrev_b32_e32 v156, 16, v94
	v_rcp_f32_e32 v162, v107
	v_add_f32_e32 v107, 1.0, v163
	v_pk_fma_f32 v[152:153], v[30:31], v[156:157], v[152:153]
	v_and_b32_e32 v99, 0xffff0000, v99
	v_and_b32_e32 v98, 0xffff0000, v98
	v_rcp_f32_e32 v163, v107
	v_mul_f32_e32 v107, 0xbfb8aa3b, v152
	v_and_b32_e32 v102, 0xffff0000, v102
	v_and_b32_e32 v103, 0xffff0000, v103
	v_exp_f32_e32 v107, v107
	v_pk_fma_f32 v[98:99], v[12:13], v[98:99], v[8:9]
	v_and_b32_e32 v165, 0xffff0000, v95
	v_pk_fma_f32 v[98:99], v[20:21], v[102:103], v[98:99]
	v_and_b32_e32 v164, 0xffff0000, v94
	v_pk_fma_f32 v[94:95], v[24:25], v[164:165], v[98:99]
	v_pk_mul_f32 v[92:93], v[92:93], v[162:163]
	v_mul_f32_e32 v98, 0xbfb8aa3b, v94
	v_exp_f32_e32 v99, v98
	v_add_f32_e32 v98, 1.0, v107
	v_mul_f32_e32 v107, 0xbfb8aa3b, v153
	v_mul_f32_e32 v162, 0xbfb8aa3b, v95
	v_exp_f32_e32 v107, v107
	v_exp_f32_e32 v163, v162
	v_add_f32_e32 v99, 1.0, v99
	v_rcp_f32_e32 v162, v99
	v_add_f32_e32 v99, 1.0, v107
	v_add_f32_e32 v107, 1.0, v163
	v_rcp_f32_e32 v163, v107
	v_rcp_f32_e32 v98, v98
	v_rcp_f32_e32 v99, v99
	v_pk_mul_f32 v[96:97], v[104:105], v[96:97]
	v_pk_mul_f32 v[94:95], v[94:95], v[162:163]
	v_pk_mul_f32 v[92:93], v[104:105], v[92:93]
	v_pk_mul_f32 v[94:95], v[104:105], v[94:95]
	v_pk_mul_f32 v[98:99], v[152:153], v[98:99]
	v_pk_mul_f32 v[98:99], v[104:105], v[98:99]
	v_cvt_pk_bf16_f32 v93, v97, v93
	v_cvt_pk_bf16_f32 v92, v96, v92
	v_lshlrev_b64 v[96:97], 11, v[144:145]
	v_cvt_pk_bf16_f32 v95, v99, v95
	v_cvt_pk_bf16_f32 v94, v98, v94
	v_lshl_add_u64 v[96:97], v[110:111], 0, v[96:97]
	global_store_dwordx4 v[96:97], v[92:95], off
	v_and_b32_e32 v99, 0xffff0000, v89
	v_and_b32_e32 v98, 0xffff0000, v88
	v_pk_fma_f32 v[92:93], v[10:11], v[150:151], v[6:7]
	v_lshlrev_b32_e32 v95, 16, v89
	v_pk_fma_f32 v[92:93], v[18:19], v[158:159], v[92:93]
	v_lshlrev_b32_e32 v94, 16, v88
	v_pk_fma_f32 v[92:93], v[22:23], v[94:95], v[92:93]
	v_pk_fma_f32 v[102:103], v[12:13], v[102:103], v[8:9]
	v_mul_f32_e32 v96, 0xbfb8aa3b, v92
	v_exp_f32_e32 v107, v96
	v_pk_fma_f32 v[96:97], v[114:115], v[100:101], v[112:113]
	v_pk_fma_f32 v[102:103], v[20:21], v[164:165], v[102:103]
	v_pk_fma_f32 v[96:97], v[4:5], v[160:161], v[96:97]
	v_and_b32_e32 v151, 0xffff0000, v91
	v_pk_fma_f32 v[88:89], v[16:17], v[98:99], v[96:97]
	v_and_b32_e32 v150, 0xffff0000, v90
	v_mul_f32_e32 v96, 0xbfb8aa3b, v88
	v_exp_f32_e32 v97, v96
	v_mul_f32_e32 v96, 0xbfb8aa3b, v93
	v_exp_f32_e32 v100, v96
	v_add_f32_e32 v96, 1.0, v107
	v_add_f32_e32 v101, 1.0, v97
	v_rcp_f32_e32 v96, v96
	v_add_f32_e32 v97, 1.0, v100
	v_mul_f32_e32 v100, 0xbfb8aa3b, v89
	v_rcp_f32_e32 v97, v97
	v_exp_f32_e32 v107, v100
	v_rcp_f32_e32 v100, v101
	v_lshlrev_b32_e32 v145, 16, v91
	v_pk_mul_f32 v[92:93], v[92:93], v[96:97]
	v_add_f32_e32 v96, 1.0, v107
	v_rcp_f32_e32 v101, v96
	v_pk_fma_f32 v[96:97], v[14:15], v[154:155], v[2:3]
	v_lshlrev_b32_e32 v144, 16, v90
	v_pk_fma_f32 v[90:91], v[24:25], v[150:151], v[102:103]
	v_pk_fma_f32 v[96:97], v[26:27], v[156:157], v[96:97]
	v_mul_f32_e32 v102, 0xbfb8aa3b, v90
	v_pk_fma_f32 v[96:97], v[30:31], v[144:145], v[96:97]
	v_exp_f32_e32 v102, v102
	v_mul_f32_e32 v107, 0xbfb8aa3b, v96
	v_exp_f32_e32 v107, v107
	v_pk_mul_f32 v[88:89], v[88:89], v[100:101]
	v_add_f32_e32 v101, 1.0, v102
	v_mul_f32_e32 v102, 0xbfb8aa3b, v97
	v_exp_f32_e32 v103, v102
	v_mul_f32_e32 v102, 0xbfb8aa3b, v91
	v_add_f32_e32 v100, 1.0, v107
	v_exp_f32_e32 v107, v102
	v_rcp_f32_e32 v102, v101
	v_add_f32_e32 v101, 1.0, v103
	v_rcp_f32_e32 v100, v100
	v_add_f32_e32 v103, 1.0, v107
	v_rcp_f32_e32 v103, v103
	v_rcp_f32_e32 v101, v101
	v_pk_mul_f32 v[92:93], v[104:105], v[92:93]
	v_pk_mul_f32 v[88:89], v[104:105], v[88:89]
	v_pk_mul_f32 v[90:91], v[90:91], v[102:103]
	v_pk_mul_f32 v[96:97], v[96:97], v[100:101]
	v_pk_mul_f32 v[90:91], v[104:105], v[90:91]
	v_pk_mul_f32 v[96:97], v[104:105], v[96:97]
	v_cvt_pk_bf16_f32 v89, v93, v89
	v_cvt_pk_bf16_f32 v88, v92, v88
	v_lshlrev_b64 v[92:93], 11, v[142:143]
	v_cvt_pk_bf16_f32 v91, v97, v91
	v_cvt_pk_bf16_f32 v90, v96, v90
	v_lshl_add_u64 v[92:93], v[110:111], 0, v[92:93]
	global_store_dwordx4 v[92:93], v[88:91], off
; __device__ __forceinline__ unsigned pk2(float lo, float hi) { return f2bf(lo) | (f2bf(hi) << 16); }
; __device__ __forceinline__ float bflo(unsigned w) { return __uint_as_float(w << 16); }
; __device__ __forceinline__ float bfhi(unsigned w) { return __uint_as_float(w & 0xffff0000u); }
; __device__ __forceinline__ float sigmoidf_(float x) { return frcp_(1.0f + fexp_(-x)); }
; __device__ __forceinline__ void p3_conv(const Args& a, const Frame& F) {
;     ...
;         for (int i = 0; i < 16; ++i) {
;             const unsigned wm[4] = {rw[i].x, rw[i].y, rw[i].z, rw[i].w}, wc_[4] = {rw[i + 1].x, rw[i + 1].y, rw[i + 1].z, rw[i + 1].w}, wp[4] = {rw[i + 2].x, rw[i + 2].y, rw[i + 2].z, rw[i + 2].w};
;             float o[8];
; #pragma unroll
;             for (int j = 0; j < 4; ++j) {
;                 const float a0 = bb[2 * j] + bflo(wm[j]) * w0[2 * j] + bflo(wc_[j]) * w1[2 * j] + bflo(wp[j]) * w2[2 * j];
;                 const float a1 = bb[2 * j + 1] + bfhi(wm[j]) * w0[2 * j + 1] + bfhi(wc_[j]) * w1[2 * j + 1] + bfhi(wp[j]) * w2[2 * j + 1];
;                 o[2 * j] = a0 * sigmoidf_(a0) * scl; o[2 * j + 1] = a1 * sigmoidf_(a1) * scl; }
;             u32x4 w; w.x = pk2(o[0], o[1]); w.y = pk2(o[2], o[3]); w.z = pk2(o[4], o[5]); w.w = pk2(o[6], o[7]);
;             *(u32x4*)(QKC + (size_t)(r0 + i) * 1024 + c0) = w;
	v_and_b32_e32 v97, 0xffff0000, v85
	v_and_b32_e32 v96, 0xffff0000, v84
	v_pk_fma_f32 v[88:89], v[10:11], v[158:159], v[6:7]
	v_lshlrev_b32_e32 v91, 16, v85
	v_pk_fma_f32 v[88:89], v[18:19], v[94:95], v[88:89]
	v_lshlrev_b32_e32 v90, 16, v84
	v_pk_fma_f32 v[88:89], v[22:23], v[90:91], v[88:89]
	v_pk_fma_f32 v[142:143], v[12:13], v[164:165], v[8:9]
	v_mul_f32_e32 v92, 0xbfb8aa3b, v88
	v_exp_f32_e32 v100, v92
	v_pk_fma_f32 v[92:93], v[114:115], v[160:161], v[112:113]
	v_lshlrev_b32_e32 v103, 16, v87
	v_pk_fma_f32 v[92:93], v[4:5], v[98:99], v[92:93]
	v_lshlrev_b32_e32 v102, 16, v86
	v_pk_fma_f32 v[84:85], v[16:17], v[96:97], v[92:93]
	v_pk_fma_f32 v[142:143], v[20:21], v[150:151], v[142:143]
	v_mul_f32_e32 v92, 0xbfb8aa3b, v84
	v_exp_f32_e32 v93, v92
	v_mul_f32_e32 v92, 0xbfb8aa3b, v89
	v_exp_f32_e32 v101, v92
	v_add_f32_e32 v92, 1.0, v100
	v_add_f32_e32 v100, 1.0, v93
	v_rcp_f32_e32 v92, v92
	v_add_f32_e32 v93, 1.0, v101
	v_mul_f32_e32 v101, 0xbfb8aa3b, v85
	v_rcp_f32_e32 v93, v93
	v_exp_f32_e32 v101, v101
	v_and_b32_e32 v153, 0xffff0000, v87
	v_and_b32_e32 v152, 0xffff0000, v86
	v_pk_mul_f32 v[88:89], v[88:89], v[92:93]
	v_add_f32_e32 v92, 1.0, v101
	v_rcp_f32_e32 v101, v92
	v_pk_fma_f32 v[92:93], v[14:15], v[156:157], v[2:3]
	v_pk_fma_f32 v[86:87], v[24:25], v[152:153], v[142:143]
	v_pk_fma_f32 v[92:93], v[26:27], v[144:145], v[92:93]
	v_mul_f32_e32 v142, 0xbfb8aa3b, v86
	v_pk_fma_f32 v[92:93], v[30:31], v[102:103], v[92:93]
	v_rcp_f32_e32 v100, v100
	v_mul_f32_e32 v107, 0xbfb8aa3b, v92
	v_exp_f32_e32 v107, v107
	v_exp_f32_e32 v142, v142
	v_pk_mul_f32 v[84:85], v[84:85], v[100:101]
	v_pk_mul_f32 v[88:89], v[104:105], v[88:89]
	v_add_f32_e32 v100, 1.0, v107
	v_add_f32_e32 v101, 1.0, v142
	v_mul_f32_e32 v107, 0xbfb8aa3b, v93
	v_mul_f32_e32 v142, 0xbfb8aa3b, v87
	v_exp_f32_e32 v107, v107
	v_exp_f32_e32 v143, v142
	v_rcp_f32_e32 v142, v101
	v_rcp_f32_e32 v100, v100
	v_add_f32_e32 v101, 1.0, v107
	v_add_f32_e32 v107, 1.0, v143
	v_rcp_f32_e32 v143, v107
	v_rcp_f32_e32 v101, v101
	v_pk_mul_f32 v[84:85], v[104:105], v[84:85]
	v_add_u32_e32 v1, s11, v1
	v_pk_mul_f32 v[86:87], v[86:87], v[142:143]
	v_pk_mul_f32 v[92:93], v[92:93], v[100:101]
	v_pk_mul_f32 v[86:87], v[104:105], v[86:87]
	v_pk_mul_f32 v[92:93], v[104:105], v[92:93]
	v_cvt_pk_bf16_f32 v85, v89, v85
	v_cvt_pk_bf16_f32 v84, v88, v84
	v_lshlrev_b64 v[88:89], 11, v[140:141]
	v_cvt_pk_bf16_f32 v87, v93, v87
	v_cvt_pk_bf16_f32 v86, v92, v86
	v_lshl_add_u64 v[88:89], v[110:111], 0, v[88:89]
	global_store_dwordx4 v[88:89], v[84:87], off
	v_and_b32_e32 v93, 0xffff0000, v81
	v_and_b32_e32 v92, 0xffff0000, v80
	v_pk_fma_f32 v[84:85], v[10:11], v[94:95], v[6:7]
	v_lshlrev_b32_e32 v87, 16, v81
	v_pk_fma_f32 v[84:85], v[18:19], v[90:91], v[84:85]
	v_lshlrev_b32_e32 v86, 16, v80
	v_pk_fma_f32 v[84:85], v[22:23], v[86:87], v[84:85]
	v_and_b32_e32 v141, 0xffff0000, v83
	v_mul_f32_e32 v88, 0xbfb8aa3b, v84
	v_exp_f32_e32 v94, v88
	v_pk_fma_f32 v[88:89], v[114:115], v[98:99], v[112:113]
	v_lshlrev_b32_e32 v99, 16, v83
	v_pk_fma_f32 v[88:89], v[4:5], v[96:97], v[88:89]
	v_lshlrev_b32_e32 v98, 16, v82
	v_pk_fma_f32 v[80:81], v[16:17], v[92:93], v[88:89]
	v_and_b32_e32 v140, 0xffff0000, v82
	v_mul_f32_e32 v88, 0xbfb8aa3b, v80
	v_exp_f32_e32 v89, v88
	v_mul_f32_e32 v88, 0xbfb8aa3b, v85
	v_exp_f32_e32 v95, v88
	v_add_f32_e32 v88, 1.0, v94
	v_add_f32_e32 v94, 1.0, v89
	v_rcp_f32_e32 v88, v88
	v_add_f32_e32 v89, 1.0, v95
	v_mul_f32_e32 v95, 0xbfb8aa3b, v81
	v_rcp_f32_e32 v89, v89
	v_exp_f32_e32 v95, v95
	v_rcp_f32_e32 v94, v94
	v_lshlrev_b64 v[28:29], 11, v[28:29]
	v_pk_mul_f32 v[84:85], v[84:85], v[88:89]
	v_add_f32_e32 v88, 1.0, v95
	v_rcp_f32_e32 v95, v88
	v_pk_fma_f32 v[88:89], v[14:15], v[144:145], v[2:3]
	v_pk_mul_f32 v[84:85], v[104:105], v[84:85]
	v_pk_fma_f32 v[88:89], v[26:27], v[102:103], v[88:89]
	v_pk_mul_f32 v[80:81], v[80:81], v[94:95]
	v_pk_fma_f32 v[88:89], v[30:31], v[98:99], v[88:89]
	v_pk_mul_f32 v[80:81], v[104:105], v[80:81]
	v_mul_f32_e32 v100, 0xbfb8aa3b, v88
	v_exp_f32_e32 v107, v100
	v_pk_fma_f32 v[100:101], v[12:13], v[150:151], v[8:9]
	v_cmp_gt_i32_e32 vcc, 0, v1
	v_pk_fma_f32 v[100:101], v[20:21], v[152:153], v[100:101]
	v_add_f32_e32 v94, 1.0, v107
	v_pk_fma_f32 v[82:83], v[24:25], v[140:141], v[100:101]
	v_rcp_f32_e32 v94, v94
	v_mul_f32_e32 v100, 0xbfb8aa3b, v82
	v_exp_f32_e32 v100, v100
	v_lshl_add_u64 v[28:29], v[110:111], 0, v[28:29]
	s_or_b64 s[6:7], vcc, s[6:7]
	v_add_u32_e32 v106, s12, v106
	v_add_f32_e32 v95, 1.0, v100
	v_mul_f32_e32 v100, 0xbfb8aa3b, v89
	v_exp_f32_e32 v101, v100
	v_mul_f32_e32 v100, 0xbfb8aa3b, v83
	v_exp_f32_e32 v107, v100
	v_rcp_f32_e32 v100, v95
	v_add_f32_e32 v95, 1.0, v101
	v_rcp_f32_e32 v95, v95
	v_add_f32_e32 v101, 1.0, v107
	v_rcp_f32_e32 v101, v101
	v_pk_mul_f32 v[88:89], v[88:89], v[94:95]
	s_nop 0
	v_pk_mul_f32 v[88:89], v[104:105], v[88:89]
	v_pk_mul_f32 v[82:83], v[82:83], v[100:101]
	v_pk_mul_f32 v[82:83], v[104:105], v[82:83]
	v_cvt_pk_bf16_f32 v81, v85, v81
	v_cvt_pk_bf16_f32 v80, v84, v80
	v_lshlrev_b64 v[84:85], 11, v[138:139]
	v_cvt_pk_bf16_f32 v83, v89, v83
	v_cvt_pk_bf16_f32 v82, v88, v82
	v_lshl_add_u64 v[84:85], v[110:111], 0, v[84:85]
	global_store_dwordx4 v[84:85], v[80:83], off
	v_and_b32_e32 v89, 0xffff0000, v77
	v_and_b32_e32 v88, 0xffff0000, v76
	v_pk_fma_f32 v[80:81], v[10:11], v[90:91], v[6:7]
	v_lshlrev_b32_e32 v83, 16, v77
	v_pk_fma_f32 v[80:81], v[18:19], v[86:87], v[80:81]
	v_lshlrev_b32_e32 v82, 16, v76
	v_pk_fma_f32 v[80:81], v[22:23], v[82:83], v[80:81]
	v_lshlrev_b32_e32 v95, 16, v79
	v_mul_f32_e32 v84, 0xbfb8aa3b, v80
	v_exp_f32_e32 v90, v84
	v_pk_fma_f32 v[84:85], v[114:115], v[96:97], v[112:113]
; __device__ __forceinline__ unsigned pk2(float lo, float hi) { return f2bf(lo) | (f2bf(hi) << 16); }
; __device__ __forceinline__ float bflo(unsigned w) { return __uint_as_float(w << 16); }
; __device__ __forceinline__ float bfhi(unsigned w) { return __uint_as_float(w & 0xffff0000u); }
; __device__ __forceinline__ float sigmoidf_(float x) { return frcp_(1.0f + fexp_(-x)); }
; __device__ __forceinline__ void p3_conv(const Args& a, const Frame& F) {
;     ...
; #pragma unroll
;         for (int i = 0; i < 16; ++i) {
;             const unsigned wm[4] = {rw[i].x, rw[i].y, rw[i].z, rw[i].w}, wc_[4] = {rw[i + 1].x, rw[i + 1].y, rw[i + 1].z, rw[i + 1].w}, wp[4] = {rw[i + 2].x, rw[i + 2].y, rw[i + 2].z, rw[i + 2].w};
;             float o[8];
; #pragma unroll
;             for (int j = 0; j < 4; ++j) {
;                 const float a0 = bb[2 * j] + bflo(wm[j]) * w0[2 * j] + bflo(wc_[j]) * w1[2 * j] + bflo(wp[j]) * w2[2 * j];
;                 const float a1 = bb[2 * j + 1] + bfhi(wm[j]) * w0[2 * j + 1] + bfhi(wc_[j]) * w1[2 * j + 1] + bfhi(wp[j]) * w2[2 * j + 1];
;                 o[2 * j] = a0 * sigmoidf_(a0) * scl; o[2 * j + 1] = a1 * sigmoidf_(a1) * scl; }
;             u32x4 w; w.x = pk2(o[0], o[1]); w.y = pk2(o[2], o[3]); w.z = pk2(o[4], o[5]); w.w = pk2(o[6], o[7]);
;             *(u32x4*)(QKC + (size_t)(r0 + i) * 1024 + c0) = w;
	v_lshlrev_b32_e32 v94, 16, v78
	v_pk_fma_f32 v[84:85], v[4:5], v[92:93], v[84:85]
	v_and_b32_e32 v101, 0xffff0000, v79
	v_pk_fma_f32 v[76:77], v[16:17], v[88:89], v[84:85]
	v_and_b32_e32 v100, 0xffff0000, v78
	v_mul_f32_e32 v84, 0xbfb8aa3b, v76
	v_exp_f32_e32 v85, v84
	v_mul_f32_e32 v84, 0xbfb8aa3b, v81
	v_exp_f32_e32 v91, v84
	v_add_f32_e32 v84, 1.0, v90
	v_add_f32_e32 v90, 1.0, v85
	v_rcp_f32_e32 v84, v84
	v_add_f32_e32 v85, 1.0, v91
	v_mul_f32_e32 v91, 0xbfb8aa3b, v77
	v_rcp_f32_e32 v85, v85
	v_exp_f32_e32 v91, v91
	v_rcp_f32_e32 v90, v90
	v_pk_mul_f32 v[80:81], v[80:81], v[84:85]
	v_add_f32_e32 v84, 1.0, v91
	v_rcp_f32_e32 v91, v84
	v_pk_fma_f32 v[84:85], v[14:15], v[102:103], v[2:3]
	v_pk_mul_f32 v[80:81], v[104:105], v[80:81]
	v_pk_fma_f32 v[84:85], v[26:27], v[98:99], v[84:85]
	v_pk_mul_f32 v[76:77], v[76:77], v[90:91]
	v_pk_fma_f32 v[84:85], v[30:31], v[94:95], v[84:85]
	v_pk_mul_f32 v[76:77], v[104:105], v[76:77]
	v_mul_f32_e32 v96, 0xbfb8aa3b, v84
	v_exp_f32_e32 v102, v96
	v_pk_fma_f32 v[96:97], v[12:13], v[152:153], v[8:9]
	v_add_f32_e32 v90, 1.0, v102
	v_pk_fma_f32 v[96:97], v[20:21], v[140:141], v[96:97]
	v_rcp_f32_e32 v90, v90
	v_pk_fma_f32 v[78:79], v[24:25], v[100:101], v[96:97]
	s_nop 0
	v_mul_f32_e32 v96, 0xbfb8aa3b, v78
	v_exp_f32_e32 v96, v96
	s_nop 0
	v_add_f32_e32 v91, 1.0, v96
	v_mul_f32_e32 v96, 0xbfb8aa3b, v85
	v_exp_f32_e32 v97, v96
	v_mul_f32_e32 v96, 0xbfb8aa3b, v79
	v_exp_f32_e32 v102, v96
	v_rcp_f32_e32 v96, v91
	v_add_f32_e32 v91, 1.0, v97
	v_rcp_f32_e32 v91, v91
	v_add_f32_e32 v97, 1.0, v102
	v_rcp_f32_e32 v97, v97
	v_pk_mul_f32 v[84:85], v[84:85], v[90:91]
	s_nop 0
	v_pk_mul_f32 v[84:85], v[104:105], v[84:85]
	v_pk_mul_f32 v[78:79], v[78:79], v[96:97]
	v_pk_mul_f32 v[78:79], v[104:105], v[78:79]
	v_cvt_pk_bf16_f32 v77, v81, v77
	v_cvt_pk_bf16_f32 v76, v80, v76
	v_lshlrev_b64 v[80:81], 11, v[136:137]
	v_cvt_pk_bf16_f32 v79, v85, v79
	v_cvt_pk_bf16_f32 v78, v84, v78
	v_lshl_add_u64 v[80:81], v[110:111], 0, v[80:81]
	global_store_dwordx4 v[80:81], v[76:79], off
	v_and_b32_e32 v85, 0xffff0000, v73
	v_and_b32_e32 v84, 0xffff0000, v72
	v_pk_fma_f32 v[76:77], v[10:11], v[86:87], v[6:7]
	v_lshlrev_b32_e32 v79, 16, v73
	v_pk_fma_f32 v[76:77], v[18:19], v[82:83], v[76:77]
	v_lshlrev_b32_e32 v78, 16, v72
	v_pk_fma_f32 v[76:77], v[22:23], v[78:79], v[76:77]
	v_lshlrev_b32_e32 v91, 16, v75
	v_mul_f32_e32 v80, 0xbfb8aa3b, v76
	v_exp_f32_e32 v86, v80
	v_pk_fma_f32 v[80:81], v[114:115], v[92:93], v[112:113]
	v_lshlrev_b32_e32 v90, 16, v74
	v_pk_fma_f32 v[80:81], v[4:5], v[88:89], v[80:81]
	v_and_b32_e32 v97, 0xffff0000, v75
	v_pk_fma_f32 v[72:73], v[16:17], v[84:85], v[80:81]
	v_and_b32_e32 v96, 0xffff0000, v74
	v_mul_f32_e32 v80, 0xbfb8aa3b, v72
	v_exp_f32_e32 v81, v80
	v_mul_f32_e32 v80, 0xbfb8aa3b, v77
	v_exp_f32_e32 v87, v80
	v_add_f32_e32 v80, 1.0, v86
	v_add_f32_e32 v86, 1.0, v81
	v_rcp_f32_e32 v80, v80
	v_add_f32_e32 v81, 1.0, v87
	v_mul_f32_e32 v87, 0xbfb8aa3b, v73
	v_rcp_f32_e32 v81, v81
	v_exp_f32_e32 v87, v87
	v_rcp_f32_e32 v86, v86
	v_pk_mul_f32 v[76:77], v[76:77], v[80:81]
	v_add_f32_e32 v80, 1.0, v87
	v_rcp_f32_e32 v87, v80
	v_pk_fma_f32 v[80:81], v[14:15], v[98:99], v[2:3]
	v_pk_mul_f32 v[76:77], v[104:105], v[76:77]
	v_pk_fma_f32 v[80:81], v[26:27], v[94:95], v[80:81]
	v_pk_mul_f32 v[72:73], v[72:73], v[86:87]
	v_pk_fma_f32 v[80:81], v[30:31], v[90:91], v[80:81]
	v_pk_mul_f32 v[72:73], v[104:105], v[72:73]
	v_mul_f32_e32 v92, 0xbfb8aa3b, v80
	v_exp_f32_e32 v98, v92
	v_pk_fma_f32 v[92:93], v[12:13], v[140:141], v[8:9]
	v_add_f32_e32 v86, 1.0, v98
	v_pk_fma_f32 v[92:93], v[20:21], v[100:101], v[92:93]
	v_rcp_f32_e32 v86, v86
	v_pk_fma_f32 v[74:75], v[24:25], v[96:97], v[92:93]
	s_nop 0
	v_mul_f32_e32 v92, 0xbfb8aa3b, v74
	v_exp_f32_e32 v92, v92
	s_nop 0
	v_add_f32_e32 v87, 1.0, v92
	v_mul_f32_e32 v92, 0xbfb8aa3b, v81
	v_exp_f32_e32 v93, v92
	v_mul_f32_e32 v92, 0xbfb8aa3b, v75
	v_exp_f32_e32 v98, v92
	v_rcp_f32_e32 v92, v87
	v_add_f32_e32 v87, 1.0, v93
	v_rcp_f32_e32 v87, v87
	v_add_f32_e32 v93, 1.0, v98
	v_rcp_f32_e32 v93, v93
	v_pk_mul_f32 v[80:81], v[80:81], v[86:87]
	s_nop 0
	v_pk_mul_f32 v[80:81], v[104:105], v[80:81]
	v_pk_mul_f32 v[74:75], v[74:75], v[92:93]
	v_pk_mul_f32 v[74:75], v[104:105], v[74:75]
	v_cvt_pk_bf16_f32 v73, v77, v73
	v_cvt_pk_bf16_f32 v72, v76, v72
	v_lshlrev_b64 v[76:77], 11, v[134:135]
	v_cvt_pk_bf16_f32 v75, v81, v75
	v_cvt_pk_bf16_f32 v74, v80, v74
	v_lshl_add_u64 v[76:77], v[110:111], 0, v[76:77]
	global_store_dwordx4 v[76:77], v[72:75], off
	v_and_b32_e32 v81, 0xffff0000, v69
	v_and_b32_e32 v80, 0xffff0000, v68
	v_pk_fma_f32 v[72:73], v[10:11], v[82:83], v[6:7]
	v_lshlrev_b32_e32 v75, 16, v69
	v_pk_fma_f32 v[72:73], v[18:19], v[78:79], v[72:73]
	v_lshlrev_b32_e32 v74, 16, v68
	v_pk_fma_f32 v[72:73], v[22:23], v[74:75], v[72:73]
	v_lshlrev_b32_e32 v87, 16, v71
	v_mul_f32_e32 v76, 0xbfb8aa3b, v72
	v_exp_f32_e32 v82, v76
	v_pk_fma_f32 v[76:77], v[114:115], v[88:89], v[112:113]
	v_lshlrev_b32_e32 v86, 16, v70
	v_pk_fma_f32 v[76:77], v[4:5], v[84:85], v[76:77]
	v_and_b32_e32 v93, 0xffff0000, v71
	v_pk_fma_f32 v[68:69], v[16:17], v[80:81], v[76:77]
	v_and_b32_e32 v92, 0xffff0000, v70
	v_mul_f32_e32 v76, 0xbfb8aa3b, v68
	v_exp_f32_e32 v77, v76
	v_mul_f32_e32 v76, 0xbfb8aa3b, v73
	v_exp_f32_e32 v83, v76
	v_add_f32_e32 v76, 1.0, v82
	v_add_f32_e32 v82, 1.0, v77
	v_rcp_f32_e32 v76, v76
	v_add_f32_e32 v77, 1.0, v83
	v_mul_f32_e32 v83, 0xbfb8aa3b, v69
	v_rcp_f32_e32 v77, v77
	v_exp_f32_e32 v83, v83
	v_rcp_f32_e32 v82, v82
	v_pk_mul_f32 v[72:73], v[72:73], v[76:77]
	v_add_f32_e32 v76, 1.0, v83
	v_rcp_f32_e32 v83, v76
	v_pk_fma_f32 v[76:77], v[14:15], v[94:95], v[2:3]
; __device__ __forceinline__ unsigned pk2(float lo, float hi) { return f2bf(lo) | (f2bf(hi) << 16); }
; __device__ __forceinline__ float bflo(unsigned w) { return __uint_as_float(w << 16); }
; __device__ __forceinline__ float bfhi(unsigned w) { return __uint_as_float(w & 0xffff0000u); }
; __device__ __forceinline__ float sigmoidf_(float x) { return frcp_(1.0f + fexp_(-x)); }
; __device__ __forceinline__ void p3_conv(const Args& a, const Frame& F) {
;     ...
; #pragma unroll
;         for (int i = 0; i < 16; ++i) {
;             const unsigned wm[4] = {rw[i].x, rw[i].y, rw[i].z, rw[i].w}, wc_[4] = {rw[i + 1].x, rw[i + 1].y, rw[i + 1].z, rw[i + 1].w}, wp[4] = {rw[i + 2].x, rw[i + 2].y, rw[i + 2].z, rw[i + 2].w};
;             float o[8];
; #pragma unroll
;             for (int j = 0; j < 4; ++j) {
;                 const float a0 = bb[2 * j] + bflo(wm[j]) * w0[2 * j] + bflo(wc_[j]) * w1[2 * j] + bflo(wp[j]) * w2[2 * j];
;                 const float a1 = bb[2 * j + 1] + bfhi(wm[j]) * w0[2 * j + 1] + bfhi(wc_[j]) * w1[2 * j + 1] + bfhi(wp[j]) * w2[2 * j + 1];
;                 o[2 * j] = a0 * sigmoidf_(a0) * scl; o[2 * j + 1] = a1 * sigmoidf_(a1) * scl; }
;             u32x4 w; w.x = pk2(o[0], o[1]); w.y = pk2(o[2], o[3]); w.z = pk2(o[4], o[5]); w.w = pk2(o[6], o[7]);
;             *(u32x4*)(QKC + (size_t)(r0 + i) * 1024 + c0) = w;
	v_pk_mul_f32 v[72:73], v[104:105], v[72:73]
	v_pk_fma_f32 v[76:77], v[26:27], v[90:91], v[76:77]
	v_pk_mul_f32 v[68:69], v[68:69], v[82:83]
	v_pk_fma_f32 v[76:77], v[30:31], v[86:87], v[76:77]
	v_pk_mul_f32 v[68:69], v[104:105], v[68:69]
	v_mul_f32_e32 v88, 0xbfb8aa3b, v76
	v_exp_f32_e32 v94, v88
	v_pk_fma_f32 v[88:89], v[12:13], v[100:101], v[8:9]
	v_add_f32_e32 v82, 1.0, v94
	v_pk_fma_f32 v[88:89], v[20:21], v[96:97], v[88:89]
	v_rcp_f32_e32 v82, v82
	v_pk_fma_f32 v[70:71], v[24:25], v[92:93], v[88:89]
	s_nop 0
	v_mul_f32_e32 v88, 0xbfb8aa3b, v70
	v_exp_f32_e32 v88, v88
	s_nop 0
	v_add_f32_e32 v83, 1.0, v88
	v_mul_f32_e32 v88, 0xbfb8aa3b, v77
	v_exp_f32_e32 v89, v88
	v_mul_f32_e32 v88, 0xbfb8aa3b, v71
	v_exp_f32_e32 v94, v88
	v_rcp_f32_e32 v88, v83
	v_add_f32_e32 v83, 1.0, v89
	v_rcp_f32_e32 v83, v83
	v_add_f32_e32 v89, 1.0, v94
	v_rcp_f32_e32 v89, v89
	v_pk_mul_f32 v[76:77], v[76:77], v[82:83]
	s_nop 0
	v_pk_mul_f32 v[76:77], v[104:105], v[76:77]
	v_pk_mul_f32 v[70:71], v[70:71], v[88:89]
	v_pk_mul_f32 v[70:71], v[104:105], v[70:71]
	v_cvt_pk_bf16_f32 v69, v73, v69
	v_cvt_pk_bf16_f32 v68, v72, v68
	v_lshlrev_b64 v[72:73], 11, v[132:133]
	v_cvt_pk_bf16_f32 v71, v77, v71
	v_cvt_pk_bf16_f32 v70, v76, v70
	v_lshl_add_u64 v[72:73], v[110:111], 0, v[72:73]
	global_store_dwordx4 v[72:73], v[68:71], off
	v_and_b32_e32 v77, 0xffff0000, v65
	v_and_b32_e32 v76, 0xffff0000, v64
	v_pk_fma_f32 v[68:69], v[10:11], v[78:79], v[6:7]
	v_lshlrev_b32_e32 v71, 16, v65
	v_pk_fma_f32 v[68:69], v[18:19], v[74:75], v[68:69]
	v_lshlrev_b32_e32 v70, 16, v64
	v_pk_fma_f32 v[68:69], v[22:23], v[70:71], v[68:69]
	v_lshlrev_b32_e32 v83, 16, v67
	v_mul_f32_e32 v72, 0xbfb8aa3b, v68
	v_exp_f32_e32 v78, v72
	v_pk_fma_f32 v[72:73], v[114:115], v[84:85], v[112:113]
	v_lshlrev_b32_e32 v82, 16, v66
	v_pk_fma_f32 v[72:73], v[4:5], v[80:81], v[72:73]
	v_and_b32_e32 v89, 0xffff0000, v67
	v_pk_fma_f32 v[64:65], v[16:17], v[76:77], v[72:73]
	v_and_b32_e32 v88, 0xffff0000, v66
	v_mul_f32_e32 v72, 0xbfb8aa3b, v64
	v_exp_f32_e32 v73, v72
	v_mul_f32_e32 v72, 0xbfb8aa3b, v69
	v_exp_f32_e32 v79, v72
	v_add_f32_e32 v72, 1.0, v78
	v_add_f32_e32 v78, 1.0, v73
	v_rcp_f32_e32 v72, v72
	v_add_f32_e32 v73, 1.0, v79
	v_mul_f32_e32 v79, 0xbfb8aa3b, v65
	v_rcp_f32_e32 v73, v73
	v_exp_f32_e32 v79, v79
	v_rcp_f32_e32 v78, v78
	v_pk_mul_f32 v[68:69], v[68:69], v[72:73]
	v_add_f32_e32 v72, 1.0, v79
	v_rcp_f32_e32 v79, v72
	v_pk_fma_f32 v[72:73], v[14:15], v[90:91], v[2:3]
	v_pk_mul_f32 v[68:69], v[104:105], v[68:69]
	v_pk_fma_f32 v[72:73], v[26:27], v[86:87], v[72:73]
	v_pk_mul_f32 v[64:65], v[64:65], v[78:79]
	v_pk_fma_f32 v[72:73], v[30:31], v[82:83], v[72:73]
	v_pk_mul_f32 v[64:65], v[104:105], v[64:65]
	v_mul_f32_e32 v84, 0xbfb8aa3b, v72
	v_exp_f32_e32 v90, v84
	v_pk_fma_f32 v[84:85], v[12:13], v[96:97], v[8:9]
	v_add_f32_e32 v78, 1.0, v90
	v_pk_fma_f32 v[84:85], v[20:21], v[92:93], v[84:85]
	v_rcp_f32_e32 v78, v78
	v_pk_fma_f32 v[66:67], v[24:25], v[88:89], v[84:85]
	s_nop 0
	v_mul_f32_e32 v84, 0xbfb8aa3b, v66
	v_exp_f32_e32 v84, v84
	s_nop 0
	v_add_f32_e32 v79, 1.0, v84
	v_mul_f32_e32 v84, 0xbfb8aa3b, v73
	v_exp_f32_e32 v85, v84
	v_mul_f32_e32 v84, 0xbfb8aa3b, v67
	v_exp_f32_e32 v90, v84
	v_rcp_f32_e32 v84, v79
	v_add_f32_e32 v79, 1.0, v85
	v_rcp_f32_e32 v79, v79
	v_add_f32_e32 v85, 1.0, v90
	v_rcp_f32_e32 v85, v85
	v_pk_mul_f32 v[72:73], v[72:73], v[78:79]
	s_nop 0
	v_pk_mul_f32 v[72:73], v[104:105], v[72:73]
	v_pk_mul_f32 v[66:67], v[66:67], v[84:85]
	v_pk_mul_f32 v[66:67], v[104:105], v[66:67]
	v_cvt_pk_bf16_f32 v65, v69, v65
	v_cvt_pk_bf16_f32 v64, v68, v64
	v_lshlrev_b64 v[68:69], 11, v[130:131]
	v_cvt_pk_bf16_f32 v67, v73, v67
	v_cvt_pk_bf16_f32 v66, v72, v66
	v_lshl_add_u64 v[68:69], v[110:111], 0, v[68:69]
	global_store_dwordx4 v[68:69], v[64:67], off
	v_and_b32_e32 v73, 0xffff0000, v61
	v_and_b32_e32 v72, 0xffff0000, v60
	v_pk_fma_f32 v[64:65], v[10:11], v[74:75], v[6:7]
	v_lshlrev_b32_e32 v67, 16, v61
	v_pk_fma_f32 v[64:65], v[18:19], v[70:71], v[64:65]
	v_lshlrev_b32_e32 v66, 16, v60
	v_pk_fma_f32 v[64:65], v[22:23], v[66:67], v[64:65]
	v_lshlrev_b32_e32 v79, 16, v63
	v_mul_f32_e32 v68, 0xbfb8aa3b, v64
	v_exp_f32_e32 v74, v68
	v_pk_fma_f32 v[68:69], v[114:115], v[80:81], v[112:113]
	v_lshlrev_b32_e32 v78, 16, v62
	v_pk_fma_f32 v[68:69], v[4:5], v[76:77], v[68:69]
	v_and_b32_e32 v85, 0xffff0000, v63
	v_pk_fma_f32 v[60:61], v[16:17], v[72:73], v[68:69]
	v_and_b32_e32 v84, 0xffff0000, v62
	v_mul_f32_e32 v68, 0xbfb8aa3b, v60
	v_exp_f32_e32 v69, v68
	v_mul_f32_e32 v68, 0xbfb8aa3b, v65
	v_exp_f32_e32 v75, v68
	v_add_f32_e32 v68, 1.0, v74
	v_add_f32_e32 v74, 1.0, v69
	v_rcp_f32_e32 v68, v68
	v_add_f32_e32 v69, 1.0, v75
	v_mul_f32_e32 v75, 0xbfb8aa3b, v61
	v_rcp_f32_e32 v69, v69
	v_exp_f32_e32 v75, v75
	v_rcp_f32_e32 v74, v74
	v_pk_mul_f32 v[64:65], v[64:65], v[68:69]
	v_add_f32_e32 v68, 1.0, v75
	v_rcp_f32_e32 v75, v68
	v_pk_fma_f32 v[68:69], v[14:15], v[86:87], v[2:3]
	v_pk_mul_f32 v[64:65], v[104:105], v[64:65]
	v_pk_fma_f32 v[68:69], v[26:27], v[82:83], v[68:69]
	v_pk_mul_f32 v[60:61], v[60:61], v[74:75]
	v_pk_fma_f32 v[68:69], v[30:31], v[78:79], v[68:69]
	v_pk_mul_f32 v[60:61], v[104:105], v[60:61]
	v_mul_f32_e32 v80, 0xbfb8aa3b, v68
	v_exp_f32_e32 v86, v80
	v_pk_fma_f32 v[80:81], v[12:13], v[92:93], v[8:9]
	v_add_f32_e32 v74, 1.0, v86
	v_pk_fma_f32 v[80:81], v[20:21], v[88:89], v[80:81]
	v_rcp_f32_e32 v74, v74
	v_pk_fma_f32 v[62:63], v[24:25], v[84:85], v[80:81]
	s_nop 0
	v_mul_f32_e32 v80, 0xbfb8aa3b, v62
	v_exp_f32_e32 v80, v80
	s_nop 0
	v_add_f32_e32 v75, 1.0, v80
	v_mul_f32_e32 v80, 0xbfb8aa3b, v69
	v_exp_f32_e32 v81, v80
	v_mul_f32_e32 v80, 0xbfb8aa3b, v63
	v_exp_f32_e32 v86, v80
; __device__ __forceinline__ unsigned pk2(float lo, float hi) { return f2bf(lo) | (f2bf(hi) << 16); }
; __device__ __forceinline__ float bflo(unsigned w) { return __uint_as_float(w << 16); }
; __device__ __forceinline__ float bfhi(unsigned w) { return __uint_as_float(w & 0xffff0000u); }
; __device__ __forceinline__ float sigmoidf_(float x) { return frcp_(1.0f + fexp_(-x)); }
; __device__ __forceinline__ void p3_conv(const Args& a, const Frame& F) {
;     ...
; #pragma unroll
;         for (int i = 0; i < 16; ++i) {
;             const unsigned wm[4] = {rw[i].x, rw[i].y, rw[i].z, rw[i].w}, wc_[4] = {rw[i + 1].x, rw[i + 1].y, rw[i + 1].z, rw[i + 1].w}, wp[4] = {rw[i + 2].x, rw[i + 2].y, rw[i + 2].z, rw[i + 2].w};
;             float o[8];
; #pragma unroll
;             for (int j = 0; j < 4; ++j) {
;                 const float a0 = bb[2 * j] + bflo(wm[j]) * w0[2 * j] + bflo(wc_[j]) * w1[2 * j] + bflo(wp[j]) * w2[2 * j];
;                 const float a1 = bb[2 * j + 1] + bfhi(wm[j]) * w0[2 * j + 1] + bfhi(wc_[j]) * w1[2 * j + 1] + bfhi(wp[j]) * w2[2 * j + 1];
;                 o[2 * j] = a0 * sigmoidf_(a0) * scl; o[2 * j + 1] = a1 * sigmoidf_(a1) * scl; }
;             u32x4 w; w.x = pk2(o[0], o[1]); w.y = pk2(o[2], o[3]); w.z = pk2(o[4], o[5]); w.w = pk2(o[6], o[7]);
;             *(u32x4*)(QKC + (size_t)(r0 + i) * 1024 + c0) = w;
	v_rcp_f32_e32 v80, v75
	v_add_f32_e32 v75, 1.0, v81
	v_rcp_f32_e32 v75, v75
	v_add_f32_e32 v81, 1.0, v86
	v_rcp_f32_e32 v81, v81
	v_pk_mul_f32 v[68:69], v[68:69], v[74:75]
	s_nop 0
	v_pk_mul_f32 v[68:69], v[104:105], v[68:69]
	v_pk_mul_f32 v[62:63], v[62:63], v[80:81]
	v_pk_mul_f32 v[62:63], v[104:105], v[62:63]
	v_cvt_pk_bf16_f32 v61, v65, v61
	v_cvt_pk_bf16_f32 v60, v64, v60
	v_lshlrev_b64 v[64:65], 11, v[128:129]
	v_cvt_pk_bf16_f32 v63, v69, v63
	v_cvt_pk_bf16_f32 v62, v68, v62
	v_lshl_add_u64 v[64:65], v[110:111], 0, v[64:65]
	global_store_dwordx4 v[64:65], v[60:63], off
	v_and_b32_e32 v69, 0xffff0000, v57
	v_and_b32_e32 v68, 0xffff0000, v56
	v_pk_fma_f32 v[60:61], v[10:11], v[70:71], v[6:7]
	v_lshlrev_b32_e32 v63, 16, v57
	v_pk_fma_f32 v[60:61], v[18:19], v[66:67], v[60:61]
	v_lshlrev_b32_e32 v62, 16, v56
	v_pk_fma_f32 v[60:61], v[22:23], v[62:63], v[60:61]
	v_lshlrev_b32_e32 v75, 16, v59
	v_mul_f32_e32 v64, 0xbfb8aa3b, v60
	v_exp_f32_e32 v70, v64
	v_pk_fma_f32 v[64:65], v[114:115], v[76:77], v[112:113]
	v_lshlrev_b32_e32 v74, 16, v58
	v_pk_fma_f32 v[64:65], v[4:5], v[72:73], v[64:65]
	v_and_b32_e32 v81, 0xffff0000, v59
	v_pk_fma_f32 v[56:57], v[16:17], v[68:69], v[64:65]
	v_and_b32_e32 v80, 0xffff0000, v58
	v_mul_f32_e32 v64, 0xbfb8aa3b, v56
	v_exp_f32_e32 v65, v64
	v_mul_f32_e32 v64, 0xbfb8aa3b, v61
	v_exp_f32_e32 v71, v64
	v_add_f32_e32 v64, 1.0, v70
	v_add_f32_e32 v70, 1.0, v65
	v_rcp_f32_e32 v64, v64
	v_add_f32_e32 v65, 1.0, v71
	v_mul_f32_e32 v71, 0xbfb8aa3b, v57
	v_rcp_f32_e32 v65, v65
	v_exp_f32_e32 v71, v71
	v_rcp_f32_e32 v70, v70
	v_pk_mul_f32 v[60:61], v[60:61], v[64:65]
	v_add_f32_e32 v64, 1.0, v71
	v_rcp_f32_e32 v71, v64
	v_pk_fma_f32 v[64:65], v[14:15], v[82:83], v[2:3]
	v_pk_mul_f32 v[60:61], v[104:105], v[60:61]
	v_pk_fma_f32 v[64:65], v[26:27], v[78:79], v[64:65]
	v_pk_mul_f32 v[56:57], v[56:57], v[70:71]
	v_pk_fma_f32 v[64:65], v[30:31], v[74:75], v[64:65]
	v_pk_mul_f32 v[56:57], v[104:105], v[56:57]
	v_mul_f32_e32 v76, 0xbfb8aa3b, v64
	v_exp_f32_e32 v82, v76
	v_pk_fma_f32 v[76:77], v[12:13], v[88:89], v[8:9]
	v_add_f32_e32 v70, 1.0, v82
	v_pk_fma_f32 v[76:77], v[20:21], v[84:85], v[76:77]
	v_rcp_f32_e32 v70, v70
	v_pk_fma_f32 v[58:59], v[24:25], v[80:81], v[76:77]
	s_nop 0
	v_mul_f32_e32 v76, 0xbfb8aa3b, v58
	v_exp_f32_e32 v76, v76
	s_nop 0
	v_add_f32_e32 v71, 1.0, v76
	v_mul_f32_e32 v76, 0xbfb8aa3b, v65
	v_exp_f32_e32 v77, v76
	v_mul_f32_e32 v76, 0xbfb8aa3b, v59
	v_exp_f32_e32 v82, v76
	v_rcp_f32_e32 v76, v71
	v_add_f32_e32 v71, 1.0, v77
	v_rcp_f32_e32 v71, v71
	v_add_f32_e32 v77, 1.0, v82
	v_rcp_f32_e32 v77, v77
	v_pk_mul_f32 v[64:65], v[64:65], v[70:71]
	s_nop 0
	v_pk_mul_f32 v[64:65], v[104:105], v[64:65]
	v_pk_mul_f32 v[58:59], v[58:59], v[76:77]
	v_pk_mul_f32 v[58:59], v[104:105], v[58:59]
	v_cvt_pk_bf16_f32 v57, v61, v57
	v_cvt_pk_bf16_f32 v56, v60, v56
	v_lshlrev_b64 v[60:61], 11, v[126:127]
	v_cvt_pk_bf16_f32 v59, v65, v59
	v_cvt_pk_bf16_f32 v58, v64, v58
	v_lshl_add_u64 v[60:61], v[110:111], 0, v[60:61]
	global_store_dwordx4 v[60:61], v[56:59], off
	v_and_b32_e32 v65, 0xffff0000, v53
	v_and_b32_e32 v64, 0xffff0000, v52
	v_pk_fma_f32 v[56:57], v[10:11], v[66:67], v[6:7]
	v_lshlrev_b32_e32 v59, 16, v53
	v_pk_fma_f32 v[56:57], v[18:19], v[62:63], v[56:57]
	v_lshlrev_b32_e32 v58, 16, v52
	v_pk_fma_f32 v[56:57], v[22:23], v[58:59], v[56:57]
	v_lshlrev_b32_e32 v71, 16, v55
	v_mul_f32_e32 v60, 0xbfb8aa3b, v56
	v_exp_f32_e32 v66, v60
	v_pk_fma_f32 v[60:61], v[114:115], v[72:73], v[112:113]
	v_lshlrev_b32_e32 v70, 16, v54
	v_pk_fma_f32 v[60:61], v[4:5], v[68:69], v[60:61]
	v_and_b32_e32 v77, 0xffff0000, v55
	v_pk_fma_f32 v[52:53], v[16:17], v[64:65], v[60:61]
	v_and_b32_e32 v76, 0xffff0000, v54
	v_mul_f32_e32 v60, 0xbfb8aa3b, v52
	v_exp_f32_e32 v61, v60
	v_mul_f32_e32 v60, 0xbfb8aa3b, v57
	v_exp_f32_e32 v67, v60
	v_add_f32_e32 v60, 1.0, v66
	v_add_f32_e32 v66, 1.0, v61
	v_rcp_f32_e32 v60, v60
	v_add_f32_e32 v61, 1.0, v67
	v_mul_f32_e32 v67, 0xbfb8aa3b, v53
	v_rcp_f32_e32 v61, v61
	v_exp_f32_e32 v67, v67
	v_rcp_f32_e32 v66, v66
	v_pk_mul_f32 v[56:57], v[56:57], v[60:61]
	v_add_f32_e32 v60, 1.0, v67
	v_rcp_f32_e32 v67, v60
	v_pk_fma_f32 v[60:61], v[14:15], v[78:79], v[2:3]
	v_pk_mul_f32 v[56:57], v[104:105], v[56:57]
	v_pk_fma_f32 v[60:61], v[26:27], v[74:75], v[60:61]
	v_pk_mul_f32 v[52:53], v[52:53], v[66:67]
	v_pk_fma_f32 v[60:61], v[30:31], v[70:71], v[60:61]
	v_pk_mul_f32 v[52:53], v[104:105], v[52:53]
	v_mul_f32_e32 v72, 0xbfb8aa3b, v60
	v_exp_f32_e32 v78, v72
	v_pk_fma_f32 v[72:73], v[12:13], v[84:85], v[8:9]
	v_add_f32_e32 v66, 1.0, v78
	v_pk_fma_f32 v[72:73], v[20:21], v[80:81], v[72:73]
	v_rcp_f32_e32 v66, v66
	v_pk_fma_f32 v[54:55], v[24:25], v[76:77], v[72:73]
	s_nop 0
	v_mul_f32_e32 v72, 0xbfb8aa3b, v54
	v_exp_f32_e32 v72, v72
	s_nop 0
	v_add_f32_e32 v67, 1.0, v72
	v_mul_f32_e32 v72, 0xbfb8aa3b, v61
	v_exp_f32_e32 v73, v72
	v_mul_f32_e32 v72, 0xbfb8aa3b, v55
	v_exp_f32_e32 v78, v72
	v_rcp_f32_e32 v72, v67
	v_add_f32_e32 v67, 1.0, v73
	v_rcp_f32_e32 v67, v67
	v_add_f32_e32 v73, 1.0, v78
	v_rcp_f32_e32 v73, v73
	v_pk_mul_f32 v[60:61], v[60:61], v[66:67]
	s_nop 0
	v_pk_mul_f32 v[60:61], v[104:105], v[60:61]
	v_pk_mul_f32 v[54:55], v[54:55], v[72:73]
	v_pk_mul_f32 v[54:55], v[104:105], v[54:55]
	v_cvt_pk_bf16_f32 v53, v57, v53
	v_cvt_pk_bf16_f32 v52, v56, v52
	v_lshlrev_b64 v[56:57], 11, v[124:125]
	v_cvt_pk_bf16_f32 v55, v61, v55
	v_cvt_pk_bf16_f32 v54, v60, v54
	v_lshl_add_u64 v[56:57], v[110:111], 0, v[56:57]
	global_store_dwordx4 v[56:57], v[52:55], off
	v_and_b32_e32 v61, 0xffff0000, v49
	v_and_b32_e32 v60, 0xffff0000, v48
	v_pk_fma_f32 v[52:53], v[10:11], v[62:63], v[6:7]
	v_lshlrev_b32_e32 v55, 16, v49
; __device__ __forceinline__ unsigned pk2(float lo, float hi) { return f2bf(lo) | (f2bf(hi) << 16); }
; __device__ __forceinline__ float bflo(unsigned w) { return __uint_as_float(w << 16); }
; __device__ __forceinline__ float bfhi(unsigned w) { return __uint_as_float(w & 0xffff0000u); }
; __device__ __forceinline__ float sigmoidf_(float x) { return frcp_(1.0f + fexp_(-x)); }
; __device__ __forceinline__ void p3_conv(const Args& a, const Frame& F) {
;     ...
; #pragma unroll
;         for (int i = 0; i < 16; ++i) {
;             const unsigned wm[4] = {rw[i].x, rw[i].y, rw[i].z, rw[i].w}, wc_[4] = {rw[i + 1].x, rw[i + 1].y, rw[i + 1].z, rw[i + 1].w}, wp[4] = {rw[i + 2].x, rw[i + 2].y, rw[i + 2].z, rw[i + 2].w};
;             float o[8];
; #pragma unroll
;             for (int j = 0; j < 4; ++j) {
;                 const float a0 = bb[2 * j] + bflo(wm[j]) * w0[2 * j] + bflo(wc_[j]) * w1[2 * j] + bflo(wp[j]) * w2[2 * j];
;                 const float a1 = bb[2 * j + 1] + bfhi(wm[j]) * w0[2 * j + 1] + bfhi(wc_[j]) * w1[2 * j + 1] + bfhi(wp[j]) * w2[2 * j + 1];
;                 o[2 * j] = a0 * sigmoidf_(a0) * scl; o[2 * j + 1] = a1 * sigmoidf_(a1) * scl; }
;             u32x4 w; w.x = pk2(o[0], o[1]); w.y = pk2(o[2], o[3]); w.z = pk2(o[4], o[5]); w.w = pk2(o[6], o[7]);
;             *(u32x4*)(QKC + (size_t)(r0 + i) * 1024 + c0) = w;
	v_pk_fma_f32 v[52:53], v[18:19], v[58:59], v[52:53]
	v_lshlrev_b32_e32 v54, 16, v48
	v_pk_fma_f32 v[52:53], v[22:23], v[54:55], v[52:53]
	v_lshlrev_b32_e32 v67, 16, v51
	v_mul_f32_e32 v56, 0xbfb8aa3b, v52
	v_exp_f32_e32 v62, v56
	v_pk_fma_f32 v[56:57], v[114:115], v[68:69], v[112:113]
	v_lshlrev_b32_e32 v66, 16, v50
	v_pk_fma_f32 v[56:57], v[4:5], v[64:65], v[56:57]
	v_and_b32_e32 v73, 0xffff0000, v51
	v_pk_fma_f32 v[48:49], v[16:17], v[60:61], v[56:57]
	v_and_b32_e32 v72, 0xffff0000, v50
	v_mul_f32_e32 v56, 0xbfb8aa3b, v48
	v_exp_f32_e32 v57, v56
	v_mul_f32_e32 v56, 0xbfb8aa3b, v53
	v_exp_f32_e32 v63, v56
	v_add_f32_e32 v56, 1.0, v62
	v_add_f32_e32 v62, 1.0, v57
	v_rcp_f32_e32 v56, v56
	v_add_f32_e32 v57, 1.0, v63
	v_mul_f32_e32 v63, 0xbfb8aa3b, v49
	v_rcp_f32_e32 v57, v57
	v_exp_f32_e32 v63, v63
	v_rcp_f32_e32 v62, v62
	v_pk_mul_f32 v[52:53], v[52:53], v[56:57]
	v_add_f32_e32 v56, 1.0, v63
	v_rcp_f32_e32 v63, v56
	v_pk_fma_f32 v[56:57], v[14:15], v[74:75], v[2:3]
	v_pk_mul_f32 v[52:53], v[104:105], v[52:53]
	v_pk_fma_f32 v[56:57], v[26:27], v[70:71], v[56:57]
	v_pk_mul_f32 v[48:49], v[48:49], v[62:63]
	v_pk_fma_f32 v[56:57], v[30:31], v[66:67], v[56:57]
	v_pk_mul_f32 v[48:49], v[104:105], v[48:49]
	v_mul_f32_e32 v68, 0xbfb8aa3b, v56
	v_exp_f32_e32 v74, v68
	v_pk_fma_f32 v[68:69], v[12:13], v[80:81], v[8:9]
	v_add_f32_e32 v62, 1.0, v74
	v_pk_fma_f32 v[68:69], v[20:21], v[76:77], v[68:69]
	v_rcp_f32_e32 v62, v62
	v_pk_fma_f32 v[50:51], v[24:25], v[72:73], v[68:69]
	s_nop 0
	v_mul_f32_e32 v68, 0xbfb8aa3b, v50
	v_exp_f32_e32 v68, v68
	s_nop 0
	v_add_f32_e32 v63, 1.0, v68
	v_mul_f32_e32 v68, 0xbfb8aa3b, v57
	v_exp_f32_e32 v69, v68
	v_mul_f32_e32 v68, 0xbfb8aa3b, v51
	v_exp_f32_e32 v74, v68
	v_rcp_f32_e32 v68, v63
	v_add_f32_e32 v63, 1.0, v69
	v_rcp_f32_e32 v63, v63
	v_add_f32_e32 v69, 1.0, v74
	v_rcp_f32_e32 v69, v69
	v_pk_mul_f32 v[56:57], v[56:57], v[62:63]
	s_nop 0
	v_pk_mul_f32 v[56:57], v[104:105], v[56:57]
	v_pk_mul_f32 v[50:51], v[50:51], v[68:69]
	v_pk_mul_f32 v[50:51], v[104:105], v[50:51]
	v_cvt_pk_bf16_f32 v49, v53, v49
	v_cvt_pk_bf16_f32 v48, v52, v48
	v_lshlrev_b64 v[52:53], 11, v[122:123]
	v_cvt_pk_bf16_f32 v51, v57, v51
	v_cvt_pk_bf16_f32 v50, v56, v50
	v_lshl_add_u64 v[52:53], v[110:111], 0, v[52:53]
	global_store_dwordx4 v[52:53], v[48:51], off
	v_and_b32_e32 v57, 0xffff0000, v45
	v_and_b32_e32 v56, 0xffff0000, v44
	v_pk_fma_f32 v[48:49], v[10:11], v[58:59], v[6:7]
	v_lshlrev_b32_e32 v51, 16, v45
	v_pk_fma_f32 v[48:49], v[18:19], v[54:55], v[48:49]
	v_lshlrev_b32_e32 v50, 16, v44
	v_pk_fma_f32 v[48:49], v[22:23], v[50:51], v[48:49]
	v_lshlrev_b32_e32 v63, 16, v47
	v_mul_f32_e32 v52, 0xbfb8aa3b, v48
	v_exp_f32_e32 v58, v52
	v_pk_fma_f32 v[52:53], v[114:115], v[64:65], v[112:113]
	v_lshlrev_b32_e32 v62, 16, v46
	v_pk_fma_f32 v[52:53], v[4:5], v[60:61], v[52:53]
	v_and_b32_e32 v69, 0xffff0000, v47
	v_pk_fma_f32 v[44:45], v[16:17], v[56:57], v[52:53]
	v_and_b32_e32 v68, 0xffff0000, v46
	v_mul_f32_e32 v52, 0xbfb8aa3b, v44
	v_exp_f32_e32 v53, v52
	v_mul_f32_e32 v52, 0xbfb8aa3b, v49
	v_exp_f32_e32 v59, v52
	v_add_f32_e32 v52, 1.0, v58
	v_add_f32_e32 v58, 1.0, v53
	v_rcp_f32_e32 v52, v52
	v_add_f32_e32 v53, 1.0, v59
	v_mul_f32_e32 v59, 0xbfb8aa3b, v45
	v_rcp_f32_e32 v53, v53
	v_exp_f32_e32 v59, v59
	v_rcp_f32_e32 v58, v58
	v_pk_mul_f32 v[48:49], v[48:49], v[52:53]
	v_add_f32_e32 v52, 1.0, v59
	v_rcp_f32_e32 v59, v52
	v_pk_fma_f32 v[52:53], v[14:15], v[70:71], v[2:3]
	v_pk_mul_f32 v[48:49], v[104:105], v[48:49]
	v_pk_fma_f32 v[52:53], v[26:27], v[66:67], v[52:53]
	v_pk_mul_f32 v[44:45], v[44:45], v[58:59]
	v_pk_fma_f32 v[52:53], v[30:31], v[62:63], v[52:53]
	v_pk_mul_f32 v[44:45], v[104:105], v[44:45]
	v_mul_f32_e32 v64, 0xbfb8aa3b, v52
	v_exp_f32_e32 v70, v64
	v_pk_fma_f32 v[64:65], v[12:13], v[76:77], v[8:9]
	v_add_f32_e32 v58, 1.0, v70
	v_pk_fma_f32 v[64:65], v[20:21], v[72:73], v[64:65]
	v_rcp_f32_e32 v58, v58
	v_pk_fma_f32 v[46:47], v[24:25], v[68:69], v[64:65]
	s_nop 0
	v_mul_f32_e32 v64, 0xbfb8aa3b, v46
	v_exp_f32_e32 v64, v64
	s_nop 0
	v_add_f32_e32 v59, 1.0, v64
	v_mul_f32_e32 v64, 0xbfb8aa3b, v53
	v_exp_f32_e32 v65, v64
	v_mul_f32_e32 v64, 0xbfb8aa3b, v47
	v_exp_f32_e32 v70, v64
	v_rcp_f32_e32 v64, v59
	v_add_f32_e32 v59, 1.0, v65
	v_rcp_f32_e32 v59, v59
	v_add_f32_e32 v65, 1.0, v70
	v_rcp_f32_e32 v65, v65
	v_pk_mul_f32 v[52:53], v[52:53], v[58:59]
	s_nop 0
	v_pk_mul_f32 v[52:53], v[104:105], v[52:53]
	v_pk_mul_f32 v[46:47], v[46:47], v[64:65]
	v_pk_mul_f32 v[46:47], v[104:105], v[46:47]
	v_cvt_pk_bf16_f32 v45, v49, v45
	v_cvt_pk_bf16_f32 v44, v48, v44
	v_lshlrev_b64 v[48:49], 11, v[120:121]
	v_cvt_pk_bf16_f32 v47, v53, v47
	v_cvt_pk_bf16_f32 v46, v52, v46
	v_lshl_add_u64 v[48:49], v[110:111], 0, v[48:49]
	global_store_dwordx4 v[48:49], v[44:47], off
	v_and_b32_e32 v53, 0xffff0000, v41
	v_and_b32_e32 v52, 0xffff0000, v40
	v_pk_fma_f32 v[44:45], v[10:11], v[54:55], v[6:7]
	v_lshlrev_b32_e32 v47, 16, v41
	v_pk_fma_f32 v[44:45], v[18:19], v[50:51], v[44:45]
	v_lshlrev_b32_e32 v46, 16, v40
	v_pk_fma_f32 v[44:45], v[22:23], v[46:47], v[44:45]
	v_lshlrev_b32_e32 v59, 16, v43
	v_mul_f32_e32 v48, 0xbfb8aa3b, v44
	v_exp_f32_e32 v54, v48
	v_pk_fma_f32 v[48:49], v[114:115], v[60:61], v[112:113]
	v_lshlrev_b32_e32 v58, 16, v42
	v_pk_fma_f32 v[48:49], v[4:5], v[56:57], v[48:49]
	v_and_b32_e32 v65, 0xffff0000, v43
	v_pk_fma_f32 v[40:41], v[16:17], v[52:53], v[48:49]
	v_and_b32_e32 v64, 0xffff0000, v42
	v_mul_f32_e32 v48, 0xbfb8aa3b, v40
	v_exp_f32_e32 v49, v48
	v_mul_f32_e32 v48, 0xbfb8aa3b, v45
	v_exp_f32_e32 v55, v48
	v_add_f32_e32 v48, 1.0, v54
	v_add_f32_e32 v54, 1.0, v49
	v_rcp_f32_e32 v48, v48
	v_add_f32_e32 v49, 1.0, v55
; __device__ __forceinline__ unsigned pk2(float lo, float hi) { return f2bf(lo) | (f2bf(hi) << 16); }
; __device__ __forceinline__ float bflo(unsigned w) { return __uint_as_float(w << 16); }
; __device__ __forceinline__ float bfhi(unsigned w) { return __uint_as_float(w & 0xffff0000u); }
; __device__ __forceinline__ float sigmoidf_(float x) { return frcp_(1.0f + fexp_(-x)); }
; __device__ __forceinline__ void p3_conv(const Args& a, const Frame& F) {
;     ...
; #pragma unroll
;         for (int i = 0; i < 16; ++i) {
;             const unsigned wm[4] = {rw[i].x, rw[i].y, rw[i].z, rw[i].w}, wc_[4] = {rw[i + 1].x, rw[i + 1].y, rw[i + 1].z, rw[i + 1].w}, wp[4] = {rw[i + 2].x, rw[i + 2].y, rw[i + 2].z, rw[i + 2].w};
;             float o[8];
; #pragma unroll
;             for (int j = 0; j < 4; ++j) {
;                 const float a0 = bb[2 * j] + bflo(wm[j]) * w0[2 * j] + bflo(wc_[j]) * w1[2 * j] + bflo(wp[j]) * w2[2 * j];
;                 const float a1 = bb[2 * j + 1] + bfhi(wm[j]) * w0[2 * j + 1] + bfhi(wc_[j]) * w1[2 * j + 1] + bfhi(wp[j]) * w2[2 * j + 1];
;                 o[2 * j] = a0 * sigmoidf_(a0) * scl; o[2 * j + 1] = a1 * sigmoidf_(a1) * scl; }
;             u32x4 w; w.x = pk2(o[0], o[1]); w.y = pk2(o[2], o[3]); w.z = pk2(o[4], o[5]); w.w = pk2(o[6], o[7]);
;             *(u32x4*)(QKC + (size_t)(r0 + i) * 1024 + c0) = w;
;         }
;     }
	v_mul_f32_e32 v55, 0xbfb8aa3b, v41
	v_rcp_f32_e32 v49, v49
	v_exp_f32_e32 v55, v55
	v_rcp_f32_e32 v54, v54
	v_pk_mul_f32 v[44:45], v[44:45], v[48:49]
	v_add_f32_e32 v48, 1.0, v55
	v_rcp_f32_e32 v55, v48
	v_pk_fma_f32 v[48:49], v[14:15], v[66:67], v[2:3]
	v_pk_mul_f32 v[44:45], v[104:105], v[44:45]
	v_pk_fma_f32 v[48:49], v[26:27], v[62:63], v[48:49]
	v_pk_mul_f32 v[40:41], v[40:41], v[54:55]
	v_pk_fma_f32 v[48:49], v[30:31], v[58:59], v[48:49]
	v_pk_mul_f32 v[40:41], v[104:105], v[40:41]
	v_mul_f32_e32 v60, 0xbfb8aa3b, v48
	v_exp_f32_e32 v66, v60
	v_pk_fma_f32 v[60:61], v[12:13], v[72:73], v[8:9]
	v_add_f32_e32 v54, 1.0, v66
	v_pk_fma_f32 v[60:61], v[20:21], v[68:69], v[60:61]
	v_rcp_f32_e32 v54, v54
	v_pk_fma_f32 v[42:43], v[24:25], v[64:65], v[60:61]
	s_nop 0
	v_mul_f32_e32 v60, 0xbfb8aa3b, v42
	v_exp_f32_e32 v60, v60
	s_nop 0
	v_add_f32_e32 v55, 1.0, v60
	v_mul_f32_e32 v60, 0xbfb8aa3b, v49
	v_exp_f32_e32 v61, v60
	v_mul_f32_e32 v60, 0xbfb8aa3b, v43
	v_exp_f32_e32 v66, v60
	v_rcp_f32_e32 v60, v55
	v_add_f32_e32 v55, 1.0, v61
	v_rcp_f32_e32 v55, v55
	v_add_f32_e32 v61, 1.0, v66
	v_rcp_f32_e32 v61, v61
	v_pk_mul_f32 v[48:49], v[48:49], v[54:55]
	s_nop 0
	v_pk_mul_f32 v[48:49], v[104:105], v[48:49]
	v_pk_mul_f32 v[42:43], v[42:43], v[60:61]
	v_pk_mul_f32 v[42:43], v[104:105], v[42:43]
	v_cvt_pk_bf16_f32 v41, v45, v41
	v_cvt_pk_bf16_f32 v40, v44, v40
	v_lshlrev_b64 v[44:45], 11, v[118:119]
	v_cvt_pk_bf16_f32 v43, v49, v43
	v_cvt_pk_bf16_f32 v42, v48, v42
	v_lshl_add_u64 v[44:45], v[110:111], 0, v[44:45]
	global_store_dwordx4 v[44:45], v[40:43], off
	v_and_b32_e32 v49, 0xffff0000, v37
	v_and_b32_e32 v48, 0xffff0000, v36
	v_pk_fma_f32 v[40:41], v[10:11], v[50:51], v[6:7]
	v_lshlrev_b32_e32 v43, 16, v37
	v_pk_fma_f32 v[40:41], v[18:19], v[46:47], v[40:41]
	v_lshlrev_b32_e32 v42, 16, v36
	v_pk_fma_f32 v[40:41], v[22:23], v[42:43], v[40:41]
	v_lshlrev_b32_e32 v55, 16, v39
	v_mul_f32_e32 v44, 0xbfb8aa3b, v40
	v_exp_f32_e32 v50, v44
	v_pk_fma_f32 v[44:45], v[114:115], v[56:57], v[112:113]
	v_lshlrev_b32_e32 v54, 16, v38
	v_pk_fma_f32 v[44:45], v[4:5], v[52:53], v[44:45]
	v_and_b32_e32 v61, 0xffff0000, v39
	v_pk_fma_f32 v[36:37], v[16:17], v[48:49], v[44:45]
	v_and_b32_e32 v60, 0xffff0000, v38
	v_mul_f32_e32 v44, 0xbfb8aa3b, v36
	v_exp_f32_e32 v45, v44
	v_mul_f32_e32 v44, 0xbfb8aa3b, v41
	v_exp_f32_e32 v51, v44
	v_add_f32_e32 v44, 1.0, v50
	v_add_f32_e32 v50, 1.0, v45
	v_rcp_f32_e32 v44, v44
	v_add_f32_e32 v45, 1.0, v51
	v_mul_f32_e32 v51, 0xbfb8aa3b, v37
	v_rcp_f32_e32 v45, v45
	v_exp_f32_e32 v51, v51
	v_rcp_f32_e32 v50, v50
	v_pk_mul_f32 v[40:41], v[40:41], v[44:45]
	v_add_f32_e32 v44, 1.0, v51
	v_rcp_f32_e32 v51, v44
	v_pk_fma_f32 v[44:45], v[14:15], v[62:63], v[2:3]
	v_pk_mul_f32 v[40:41], v[104:105], v[40:41]
	v_pk_fma_f32 v[44:45], v[26:27], v[58:59], v[44:45]
	v_pk_mul_f32 v[36:37], v[36:37], v[50:51]
	v_pk_fma_f32 v[44:45], v[30:31], v[54:55], v[44:45]
	v_pk_mul_f32 v[36:37], v[104:105], v[36:37]
	v_mul_f32_e32 v56, 0xbfb8aa3b, v44
	v_exp_f32_e32 v62, v56
	v_pk_fma_f32 v[56:57], v[12:13], v[68:69], v[8:9]
	v_add_f32_e32 v50, 1.0, v62
	v_pk_fma_f32 v[56:57], v[20:21], v[64:65], v[56:57]
	v_rcp_f32_e32 v50, v50
	v_pk_fma_f32 v[38:39], v[24:25], v[60:61], v[56:57]
	s_nop 0
	v_mul_f32_e32 v56, 0xbfb8aa3b, v38
	v_exp_f32_e32 v56, v56
	s_nop 0
	v_add_f32_e32 v51, 1.0, v56
	v_mul_f32_e32 v56, 0xbfb8aa3b, v45
	v_exp_f32_e32 v57, v56
	v_mul_f32_e32 v56, 0xbfb8aa3b, v39
	v_exp_f32_e32 v62, v56
	v_rcp_f32_e32 v56, v51
	v_add_f32_e32 v51, 1.0, v57
	v_rcp_f32_e32 v51, v51
	v_add_f32_e32 v57, 1.0, v62
	v_rcp_f32_e32 v57, v57
	v_pk_mul_f32 v[44:45], v[44:45], v[50:51]
	s_nop 0
	v_pk_mul_f32 v[44:45], v[104:105], v[44:45]
	v_pk_mul_f32 v[38:39], v[38:39], v[56:57]
	v_pk_mul_f32 v[38:39], v[104:105], v[38:39]
	v_cvt_pk_bf16_f32 v37, v41, v37
	v_cvt_pk_bf16_f32 v36, v40, v36
	v_lshlrev_b64 v[40:41], 11, v[116:117]
	v_cvt_pk_bf16_f32 v39, v45, v39
	v_cvt_pk_bf16_f32 v38, v44, v38
	v_lshl_add_u64 v[40:41], v[110:111], 0, v[40:41]
	global_store_dwordx4 v[40:41], v[36:39], off
	s_nop 1
	v_pk_fma_f32 v[36:37], v[10:11], v[46:47], v[6:7]
	v_lshlrev_b32_e32 v39, 16, v33
	v_pk_fma_f32 v[36:37], v[18:19], v[42:43], v[36:37]
	v_lshlrev_b32_e32 v38, 16, v32
	v_pk_fma_f32 v[36:37], v[22:23], v[38:39], v[36:37]
	v_and_b32_e32 v33, 0xffff0000, v33
	v_mul_f32_e32 v38, 0xbfb8aa3b, v36
	v_exp_f32_e32 v40, v38
	v_pk_fma_f32 v[38:39], v[114:115], v[52:53], v[112:113]
	v_and_b32_e32 v32, 0xffff0000, v32
	v_pk_fma_f32 v[38:39], v[4:5], v[48:49], v[38:39]
	v_lshlrev_b32_e32 v43, 16, v35
	v_pk_fma_f32 v[32:33], v[16:17], v[32:33], v[38:39]
	v_lshlrev_b32_e32 v42, 16, v34
	v_mul_f32_e32 v38, 0xbfb8aa3b, v32
	v_exp_f32_e32 v39, v38
	v_mul_f32_e32 v38, 0xbfb8aa3b, v37
	v_exp_f32_e32 v41, v38
	v_add_f32_e32 v38, 1.0, v40
	v_add_f32_e32 v40, 1.0, v39
	v_rcp_f32_e32 v38, v38
	v_add_f32_e32 v39, 1.0, v41
	v_mul_f32_e32 v41, 0xbfb8aa3b, v33
	v_rcp_f32_e32 v39, v39
	v_exp_f32_e32 v41, v41
	v_and_b32_e32 v35, 0xffff0000, v35
	v_and_b32_e32 v34, 0xffff0000, v34
	v_pk_mul_f32 v[36:37], v[36:37], v[38:39]
	v_add_f32_e32 v38, 1.0, v41
	v_rcp_f32_e32 v41, v38
	v_pk_fma_f32 v[38:39], v[14:15], v[58:59], v[2:3]
	v_rcp_f32_e32 v40, v40
	v_pk_fma_f32 v[38:39], v[26:27], v[54:55], v[38:39]
	v_pk_mul_f32 v[36:37], v[104:105], v[36:37]
	v_pk_fma_f32 v[38:39], v[30:31], v[42:43], v[38:39]
	v_pk_mul_f32 v[32:33], v[32:33], v[40:41]
	v_mul_f32_e32 v42, 0xbfb8aa3b, v38
	v_exp_f32_e32 v44, v42
	v_pk_fma_f32 v[42:43], v[12:13], v[64:65], v[8:9]
	v_pk_mul_f32 v[32:33], v[104:105], v[32:33]
	v_pk_fma_f32 v[42:43], v[20:21], v[60:61], v[42:43]
	v_add_f32_e32 v40, 1.0, v44
	v_pk_fma_f32 v[34:35], v[24:25], v[34:35], v[42:43]
	v_rcp_f32_e32 v40, v40
	v_mul_f32_e32 v42, 0xbfb8aa3b, v34
	v_exp_f32_e32 v42, v42
	s_nop 0
	v_add_f32_e32 v41, 1.0, v42
	v_mul_f32_e32 v42, 0xbfb8aa3b, v39
	v_exp_f32_e32 v43, v42
	v_mul_f32_e32 v42, 0xbfb8aa3b, v35
	v_exp_f32_e32 v44, v42
	v_rcp_f32_e32 v42, v41
	v_add_f32_e32 v41, 1.0, v43
	v_rcp_f32_e32 v41, v41
	v_add_f32_e32 v43, 1.0, v44
	v_rcp_f32_e32 v43, v43
	v_pk_mul_f32 v[38:39], v[38:39], v[40:41]
	s_nop 0
	v_pk_mul_f32 v[38:39], v[104:105], v[38:39]
	v_pk_mul_f32 v[34:35], v[34:35], v[42:43]
	v_pk_mul_f32 v[34:35], v[104:105], v[34:35]
	v_cvt_pk_bf16_f32 v35, v39, v35
	v_cvt_pk_bf16_f32 v34, v38, v34
	v_cvt_pk_bf16_f32 v33, v37, v33
	v_cvt_pk_bf16_f32 v32, v36, v32
	global_store_dwordx4 v[28:29], v[32:35], off
	s_andn2_b64 exec, exec, s[6:7]
	s_cbranch_execz .LBB0_380
